# queue-claim pre-issue as before, with 52 bytes of unreachable padding so every K-loop head has the same address modulo 64 as in the best version
# speedup vs baseline: 1.0085x; 1.0085x over previous
.LBB0_340:
	s_mov_b64 s[42:43], 0x80
	s_add_i32 m0, s83, 0x18000
	v_lshl_add_u64 v[6:7], v[6:7], 0, s[42:43]
	s_waitcnt vmcnt(2)
	s_barrier
	global_load_lds_dwordx4 v[6:7], off
	v_lshl_add_u64 v[4:5], v[4:5], 0, s[42:43]
	s_add_i32 m0, s83, 0x1a000
	s_add_i32 s87, s83, 0x8000
	s_add_i32 s88, s83, 0xa000
	global_load_lds_dwordx4 v[4:5], off
	v_lshl_add_u64 v[0:1], v[0:1], 0, s[42:43]
	s_mov_b32 m0, s87
	s_add_u32 s10, s8, 0x40080
	global_load_lds_dwordx4 v[0:1], off
	v_lshl_add_u64 v[0:1], v[2:3], 0, s[42:43]
	s_mov_b32 m0, s88
	s_addc_u32 s11, s9, 0
	global_load_lds_dwordx4 v[0:1], off
	s_add_i32 m0, s83, 0x1c000
	v_lshl_add_u64 v[0:1], s[10:11], 0, v[162:163]
	global_load_lds_dwordx4 v[0:1], off
	v_lshl_add_u64 v[0:1], s[10:11], 0, v[166:167]
	s_add_i32 m0, s83, 0x1e000
	s_waitcnt vmcnt(0)
	v_and_b32_e32 v16, 15, v8
	global_load_lds_dwordx4 v[0:1], off
	v_lshlrev_b32_e32 v0, 14, v9
	v_and_b32_e32 v0, 0xffff8000, v0
	v_lshl_add_u32 v0, v10, 11, v0
	v_and_b32_e32 v1, 1, v9
	v_or_b32_e32 v17, s39, v16
	v_lshl_or_b32 v0, v1, 6, v0
	v_lshlrev_b32_e32 v18, 6, v17
	v_and_b32_e32 v19, 48, v8
	s_movk_i32 s5, 0x3c0
	v_lshl_add_u32 v170, v11, 1, v0
	v_lshlrev_b32_e32 v0, 14, v12
	v_and_or_b32 v18, v18, s5, v19
	v_readlane_b32 s5, v251, 16
	v_and_b32_e32 v0, 0xffff8000, v0
	v_and_b32_e32 v15, 0xfffffc00, v15
	v_lshlrev_b32_e32 v17, 2, v17
	v_lshlrev_b32_e32 v8, 2, v8
	s_cmpk_lt_u32 s5, 0x100
	v_lshl_add_u32 v0, v13, 11, v0
	v_and_b32_e32 v1, 1, v12
	v_add_u32_e32 v20, s63, v15
	v_and_b32_e32 v17, 32, v17
	v_lshl_or_b32 v16, v16, 6, v19
	v_add_u32_e32 v15, s65, v15
	v_and_b32_e32 v8, 32, v8
	s_waitcnt vmcnt(6)
	s_cselect_b64 s[44:45], -1, 0
	s_cmp_eq_u32 s61, 0
	v_lshl_or_b32 v0, v1, 6, v0
	v_bitop3_b32 v17, v18, v20, v17 bitop3:0xde
	v_bitop3_b32 v182, v16, v15, v8 bitop3:0xde
	s_cselect_b64 s[46:47], -1, 0
	v_lshl_add_u32 v172, v14, 1, v0
	s_add_i32 s89, 0, 0x10000
	s_add_i32 s90, 0, 0x14000
	v_mbcnt_lo_u32_b32 v0, -1, 0
	v_mov_b32_e32 v171, v169
	v_mov_b32_e32 v173, v169
	v_add_u32_e32 v183, s89, v182
	v_add_u32_e32 v184, s90, v182
	v_add_u32_e32 v185, 0, v17
	s_mov_b32 s48, 0x39000000
	s_mov_b32 s50, 0x3e6d3388
	s_mov_b32 s52, 0x3f07dc22
	s_mov_b32 s54, 0xbf3a00e3
	s_mov_b32 s56, 0x3f35f0e3
	s_mov_b32 s58, 0xbe11a98e
	s_mov_b32 s60, 0x3e027906
	s_mov_b32 s62, 0xbf38aa3b
	s_mov_b32 s64, 0xb938aa3b
	v_mbcnt_hi_u32_b32 v186, -1, v0
	s_barrier
	s_branch .LBB0_343
	s_nop 0
	s_nop 0
	s_nop 0
	s_nop 0
	s_nop 0
	s_nop 0
	s_nop 0
	s_nop 0
	s_nop 0
	s_nop 0
	s_nop 0
	s_nop 0
	s_nop 0
